# gate-phase row-factor loads batched; prep_tok rdsa loads batched
# speedup vs baseline: 1.0141x; 1.0004x over previous
.LBB0_1825:
	v_mov_b64_e32 v[6:7], 0x57f
	v_cmp_gt_i64_e32 vcc, s[8:9], v[6:7]
	s_mov_b64 s[10:11], -1
	s_cbranch_vccnz .LBB0_1824
	s_ashr_i32 s10, s8, 31
	s_lshr_b32 s10, s10, 29
	s_add_i32 s10, s8, s10
	s_ashr_i32 s11, s10, 3
	s_and_b32 s10, s10, -8
	s_sub_i32 s10, s8, s10
	s_cmp_lt_i32 s10, 0
	s_movk_i32 s12, 0xb1
	s_cselect_b32 s12, s12, 0xb0
	s_mul_i32 s10, s12, s10
	s_add_i32 s10, s10, s11
	s_mul_hi_i32 s11, s10, 0x2e8ba2e9
	s_lshr_b32 s12, s11, 31
	s_ashr_i32 s11, s11, 5
	s_add_i32 s11, s11, s12
	s_lshl_b32 s12, s11, 3
	s_sub_i32 s14, 64, s12
	s_min_i32 s14, s14, 8
	s_abs_i32 s14, s14
	v_cvt_f32_u32_e32 v2, s14
	s_sub_i32 s15, 0, s14
	s_mulk_i32 s11, 0xb0
	s_sub_i32 s10, s10, s11
	v_rcp_iflag_f32_e32 v2, v2
	s_ashr_i32 s11, s10, 31
	s_abs_i32 s10, s10
	v_mul_f32_e32 v2, 0x4f7ffffe, v2
	v_cvt_u32_f32_e32 v2, v2
	s_nop 0
	v_readfirstlane_b32 s16, v2
	s_mul_i32 s15, s15, s16
	s_mul_hi_u32 s15, s16, s15
	s_add_i32 s16, s16, s15
	s_mul_hi_u32 s15, s10, s16
	s_mul_i32 s15, s15, s14
	s_sub_i32 s10, s10, s15
	s_sub_i32 s15, s10, s14
	s_cmp_ge_u32 s10, s14
	s_cselect_b32 s10, s15, s10
	s_sub_i32 s15, s10, s14
	s_cmp_ge_u32 s10, s14
	s_cselect_b32 s10, s15, s10
	s_xor_b32 s10, s10, s11
	s_sub_i32 s10, s10, s11
	s_add_i32 s12, s10, s12
	s_cmp_eq_u32 s12, s13
	s_cbranch_scc1 .LBB0_1823
	v_lshl_add_u32 v6, s12, 8, v9
	v_ashrrev_i32_e32 v7, 31, v6
	s_waitcnt lgkmcnt(0)
	v_lshlrev_b64 v[10:11], 7, v[6:7]
	v_lshl_add_u64 v[14:15], v[4:5], 0, v[10:11]
	global_load_dwordx4 v[10:13], v[14:15], off
	global_load_dwordx4 v[16:19], v[14:15], off offset:16
	global_load_dwordx4 v[20:23], v[14:15], off offset:32
	global_load_dwordx4 v[24:27], v[14:15], off offset:48
	s_waitcnt vmcnt(3) lgkmcnt(0)
	v_add_f32_e32 v2, v10, v11
	v_add_f32_e32 v10, v12, v13
	v_add_f32_e32 v2, v2, v10
	v_add_f32_e32 v2, 0, v2
	s_waitcnt vmcnt(2)
	v_add_f32_e32 v10, v16, v17
	v_add_f32_e32 v11, v18, v19
	v_add_f32_e32 v10, v10, v11
	v_add_f32_e32 v2, v2, v10
	s_waitcnt vmcnt(1)
	v_add_f32_e32 v10, v20, v21
	v_add_f32_e32 v11, v22, v23
	v_add_f32_e32 v10, v10, v11
	v_add_f32_e32 v2, v2, v10
	s_waitcnt vmcnt(0)
	v_add_f32_e32 v10, v24, v25
	v_add_f32_e32 v11, v26, v27
	v_add_f32_e32 v10, v10, v11
	v_add_f32_e32 v2, v2, v10
	v_xor_b32_e32 v10, 1, v230
	v_cmp_lt_i32_e32 vcc, v10, v231
	s_nop 1
	v_cndmask_b32_e32 v10, v230, v10, vcc
	v_lshlrev_b32_e32 v10, 2, v10
	ds_bpermute_b32 v10, v10, v2
	s_and_saveexec_b64 s[10:11], s[0:1]
	s_cbranch_execz .LBB0_1822
	s_waitcnt lgkmcnt(0)
	v_add_f32_e32 v2, v2, v10
	v_fmamk_f32 v2, v2, 0x3a000000, v241
	v_mul_f32_e32 v10, 0x4b800000, v2
	v_cmp_gt_f32_e32 vcc, s25, v2
	v_lshl_add_u64 v[6:7], v[6:7], 2, s[6:7]
	s_nop 0
	v_cndmask_b32_e32 v2, v2, v10, vcc
	v_rsq_f32_e32 v2, v2
	s_nop 0
	v_mul_f32_e32 v10, 0x45800000, v2
	v_cndmask_b32_e32 v2, v2, v10, vcc
	global_store_dword v[6:7], v2, off
	s_branch .LBB0_1822
